# v066 + packed->plain f32 in attention rescale paths and unit epilogues (192 sites)
# baseline (speedup 1.0000x reference)
; __device__ __forceinline__ int crow(int r, int hi) { return (r & 3) + 8 * (r >> 2) + 4 * hi; }
; __device__ __forceinline__ void smax_tile(f32x16& p0, f32x16& p1, float& mhat, float& l_reg, f32x16 (&o)[4], float* al_l, const bool first, int r32, int hi,
;                                           bf16x8& pa0, bf16x8& pa1, bf16x8& pa2, bf16x8& pa3) {
;     ...
;         if (!first) { const float f = __builtin_amdgcn_exp2f(-dl); l_reg *= f;
;             if (hi == 0) al_l[r32] = f; asm volatile("s_waitcnt lgkmcnt(0)" ::: "memory");
; #pragma unroll
;             for (int d = 0; d < 4; ++d)
; #pragma unroll
;                 for (int r = 0; r < 16; ++r) o[d][r] *= al_l[crow(r, hi)]; }
.LBB0_603:
	s_or_b64 exec, exec, s[46:47]
	v_mul_f32_e32 v204, v204, v161
	s_waitcnt lgkmcnt(0)
	v_add_u32_e32 v161, s67, v177
	ds_read_b128 v[162:165], v161 offset:128
	ds_read_b128 v[166:169], v161 offset:160
	ds_read_b128 v[170:173], v161 offset:192
	ds_read_b128 v[208:211], v161 offset:224
	s_waitcnt lgkmcnt(0)
	v_mul_f32_e32 v66, v66, v164
	v_mul_f32_e32 v67, v67, v165
	v_mul_f32_e32 v68, v68, v166
	v_mul_f32_e32 v69, v69, v167
	v_mul_f32_e32 v72, v72, v170
	v_mul_f32_e32 v73, v73, v171
	v_mul_f32_e32 v76, v76, v208
	v_mul_f32_e32 v77, v77, v209
	v_mul_f32_e32 v78, v78, v210
	v_mul_f32_e32 v79, v79, v211
	v_mul_f32_e32 v74, v74, v172
	v_mul_f32_e32 v75, v75, v173
	v_mul_f32_e32 v70, v70, v168
	v_mul_f32_e32 v71, v71, v169
	v_mul_f32_e32 v64, v64, v162
	v_mul_f32_e32 v65, v65, v163
	v_mul_f32_e32 v60, v60, v208
	v_mul_f32_e32 v61, v61, v209
	v_mul_f32_e32 v56, v56, v170
	v_mul_f32_e32 v57, v57, v171
	v_mul_f32_e32 v52, v52, v166
	v_mul_f32_e32 v53, v53, v167
	v_mul_f32_e32 v62, v62, v210
	v_mul_f32_e32 v63, v63, v211
	v_mul_f32_e32 v58, v58, v172
	v_mul_f32_e32 v59, v59, v173
	v_mul_f32_e32 v54, v54, v168
	v_mul_f32_e32 v55, v55, v169
	v_mul_f32_e32 v50, v50, v164
	v_mul_f32_e32 v51, v51, v165
	v_mul_f32_e32 v48, v48, v162
	v_mul_f32_e32 v49, v49, v163
	v_mul_f32_e32 v44, v44, v208
	v_mul_f32_e32 v45, v45, v209
	v_mul_f32_e32 v40, v40, v170
	v_mul_f32_e32 v41, v41, v171
	v_mul_f32_e32 v36, v36, v166
	v_mul_f32_e32 v37, v37, v167
	v_mul_f32_e32 v46, v46, v210
	v_mul_f32_e32 v47, v47, v211
	v_mul_f32_e32 v42, v42, v172
	v_mul_f32_e32 v43, v43, v173
	v_mul_f32_e32 v38, v38, v168
	v_mul_f32_e32 v39, v39, v169
	v_mul_f32_e32 v34, v34, v164
	v_mul_f32_e32 v35, v35, v165
	v_mul_f32_e32 v32, v32, v162
	v_mul_f32_e32 v33, v33, v163
	v_mul_f32_e32 v28, v28, v208
	v_mul_f32_e32 v29, v29, v209
	v_mul_f32_e32 v24, v24, v170
	v_mul_f32_e32 v25, v25, v171
	v_mul_f32_e32 v20, v20, v166
	v_mul_f32_e32 v21, v21, v167
	v_mul_f32_e32 v30, v30, v210
	v_mul_f32_e32 v31, v31, v211
	v_mul_f32_e32 v26, v26, v172
	v_mul_f32_e32 v27, v27, v173
	v_mul_f32_e32 v22, v22, v168
	v_mul_f32_e32 v23, v23, v169
	v_mul_f32_e32 v18, v18, v164
	v_mul_f32_e32 v19, v19, v165
	v_mul_f32_e32 v16, v16, v162
	v_mul_f32_e32 v17, v17, v163

; __device__ __forceinline__ int crow(int r, int hi) { return (r & 3) + 8 * (r >> 2) + 4 * hi; }
; __device__ __forceinline__ void smax_tile(f32x16& p0, f32x16& p1, float& mhat, float& l_reg, f32x16 (&o)[4], float* al_l, const bool first, int r32, int hi,
;                                           bf16x8& pa0, bf16x8& pa1, bf16x8& pa2, bf16x8& pa3) {
;     ...
;     if (__builtin_expect(first || __any(rm > THRL), 0)) {
;         const float dl = first ? rm : fmaxf(rm, 0.f);
;         mhat += dl;
; #pragma unroll
;         for (int r = 0; r < 16; ++r) { p0[r] -= dl; p1[r] -= dl; }
;         if (!first) { const float f = __builtin_amdgcn_exp2f(-dl); l_reg *= f;
;             if (hi == 0) al_l[r32] = f; asm volatile("s_waitcnt lgkmcnt(0)" ::: "memory");
; #pragma unroll
;             for (int d = 0; d < 4; ++d)
; #pragma unroll
;                 for (int r = 0; r < 16; ++r) o[d][r] *= al_l[crow(r, hi)]; }
.LBB0_635:
	v_max_f32_e32 v122, v122, v122
	v_max_f32_e32 v122, 0, v122
	v_exp_f32_e64 v123, -v122
	s_and_saveexec_b64 s[38:39], s[10:11]
	ds_write_b32 v201, v123 offset:128
	s_or_b64 exec, exec, s[38:39]
	s_waitcnt lgkmcnt(0)
	v_add_u32_e32 v134, s67, v177
	v_add_f32_e32 v203, v203, v122
	v_add_f32_e64 v96, v96, -v122
	v_add_f32_e64 v97, v97, -v122
	v_add_f32_e64 v80, v80, -v122
	v_add_f32_e64 v81, v81, -v122
	v_add_f32_e64 v98, v98, -v122
	v_add_f32_e64 v99, v99, -v122
	v_add_f32_e64 v82, v82, -v122
	v_add_f32_e64 v83, v83, -v122
	v_add_f32_e64 v100, v100, -v122
	v_add_f32_e64 v101, v101, -v122
	v_add_f32_e64 v84, v84, -v122
	v_add_f32_e64 v85, v85, -v122
	v_add_f32_e64 v102, v102, -v122
	v_add_f32_e64 v103, v103, -v122
	v_add_f32_e64 v86, v86, -v122
	v_add_f32_e64 v87, v87, -v122
	v_add_f32_e64 v104, v104, -v122
	v_add_f32_e64 v105, v105, -v122
	v_add_f32_e64 v88, v88, -v122
	v_add_f32_e64 v89, v89, -v122
	v_add_f32_e64 v106, v106, -v122
	v_add_f32_e64 v107, v107, -v122
	v_add_f32_e64 v90, v90, -v122
	v_add_f32_e64 v91, v91, -v122
	v_add_f32_e64 v108, v108, -v122
	v_add_f32_e64 v109, v109, -v122
	v_add_f32_e64 v92, v92, -v122
	v_add_f32_e64 v93, v93, -v122
	v_add_f32_e64 v110, v110, -v122
	v_add_f32_e64 v111, v111, -v122
	v_add_f32_e64 v94, v94, -v122
	v_add_f32_e64 v95, v95, -v122
	v_mul_f32_e32 v204, v204, v123
	ds_read_b128 v[122:125], v134 offset:128
	ds_read_b128 v[126:129], v134 offset:160
	ds_read_b128 v[130:133], v134 offset:192
	ds_read_b128 v[134:137], v134 offset:224
	s_waitcnt lgkmcnt(0)
	v_mul_f32_e32 v66, v66, v124
	v_mul_f32_e32 v67, v67, v125
	v_mul_f32_e32 v68, v68, v126
	v_mul_f32_e32 v69, v69, v127
	v_mul_f32_e32 v72, v72, v130
	v_mul_f32_e32 v73, v73, v131
	v_mul_f32_e32 v76, v76, v134
	v_mul_f32_e32 v77, v77, v135
	v_mul_f32_e32 v78, v78, v136
	v_mul_f32_e32 v79, v79, v137
	v_mul_f32_e32 v74, v74, v132
	v_mul_f32_e32 v75, v75, v133
	v_mul_f32_e32 v70, v70, v128
	v_mul_f32_e32 v71, v71, v129
	v_mul_f32_e32 v64, v64, v122
	v_mul_f32_e32 v65, v65, v123
	v_mul_f32_e32 v60, v60, v134
	v_mul_f32_e32 v61, v61, v135
	v_mul_f32_e32 v56, v56, v130
	v_mul_f32_e32 v57, v57, v131
	v_mul_f32_e32 v52, v52, v126
	v_mul_f32_e32 v53, v53, v127
	v_mul_f32_e32 v62, v62, v136
	v_mul_f32_e32 v63, v63, v137
	v_mul_f32_e32 v58, v58, v132
	v_mul_f32_e32 v59, v59, v133
	v_mul_f32_e32 v54, v54, v128
	v_mul_f32_e32 v55, v55, v129
	v_mul_f32_e32 v50, v50, v124
	v_mul_f32_e32 v51, v51, v125
	v_mul_f32_e32 v48, v48, v122
	v_mul_f32_e32 v49, v49, v123
	v_mul_f32_e32 v44, v44, v134
	v_mul_f32_e32 v45, v45, v135
	v_mul_f32_e32 v40, v40, v130
	v_mul_f32_e32 v41, v41, v131
	v_mul_f32_e32 v36, v36, v126
	v_mul_f32_e32 v37, v37, v127
	v_mul_f32_e32 v46, v46, v136
	v_mul_f32_e32 v47, v47, v137
	v_mul_f32_e32 v42, v42, v132
	v_mul_f32_e32 v43, v43, v133
	v_mul_f32_e32 v38, v38, v128
	v_mul_f32_e32 v39, v39, v129
	v_mul_f32_e32 v34, v34, v124
	v_mul_f32_e32 v35, v35, v125
	v_mul_f32_e32 v32, v32, v122
	v_mul_f32_e32 v33, v33, v123
	v_mul_f32_e32 v28, v28, v134
	v_mul_f32_e32 v29, v29, v135
	v_mul_f32_e32 v24, v24, v130
	v_mul_f32_e32 v25, v25, v131
	v_mul_f32_e32 v20, v20, v126
	v_mul_f32_e32 v21, v21, v127
	v_mul_f32_e32 v30, v30, v136
	v_mul_f32_e32 v31, v31, v137
	v_mul_f32_e32 v26, v26, v132
	v_mul_f32_e32 v27, v27, v133
	v_mul_f32_e32 v22, v22, v128
	v_mul_f32_e32 v23, v23, v129
	v_mul_f32_e32 v18, v18, v124
	v_mul_f32_e32 v19, v19, v125
	v_mul_f32_e32 v16, v16, v122
	v_mul_f32_e32 v17, v17, v123
	s_branch .LBB0_624

; __global__ void __launch_bounds__(512, 2) hymba_fwd(Args args) {
;     ...
;             if (j == 0) {
; #pragma unroll
;                 for (int d0 = 0; d0 < 4; ++d0)
; #pragma unroll
;                     for (int rg = 0; rg < 4; ++rg) { f32x4 w; w[0] = o[d0][4 * rg] * rli[4 * rg]; w[1] = o[d0][4 * rg + 1] * rli[4 * rg + 1]; w[2] = o[d0][4 * rg + 2] * rli[4 * rg + 2]; w[3] = o[d0][4 * rg + 3] * rli[4 * rg + 3];
;                         st4[(d0 * 4 + rg) * 64] = w; }
.LBB0_640:
	v_mul_f32_e32 v64, v64, v146
	v_mul_f32_e32 v65, v65, v147
	v_mul_f32_e32 v66, v66, v144
	v_mul_f32_e32 v67, v67, v145
	global_store_dwordx4 v[148:149], v[64:67], off
	s_movk_i32 s10, 0x1000
	v_mul_f32_e32 v32, v32, v146
	v_mul_f32_e32 v33, v33, v147
	v_mul_f32_e32 v64, v68, v132
	v_mul_f32_e32 v65, v69, v133
	v_mul_f32_e32 v66, v70, v142
	v_mul_f32_e32 v67, v71, v143
	global_store_dwordx4 v[148:149], v[64:67], off offset:1024
	v_mul_f32_e32 v34, v34, v144
	v_mul_f32_e32 v35, v35, v145
	v_mul_f32_e32 v48, v48, v146
	v_mul_f32_e32 v49, v49, v147
	v_mul_f32_e32 v64, v72, v140
	v_mul_f32_e32 v65, v73, v141
	v_mul_f32_e32 v66, v74, v134
	v_mul_f32_e32 v67, v75, v135
	global_store_dwordx4 v[148:149], v[64:67], off offset:2048
	v_mul_f32_e32 v50, v50, v144
	v_mul_f32_e32 v51, v51, v145
	v_mul_f32_e32 v16, v16, v146
	v_mul_f32_e32 v17, v17, v147
	v_mul_f32_e32 v64, v76, v130
	v_mul_f32_e32 v65, v77, v131
	v_mul_f32_e32 v66, v78, v128
	v_mul_f32_e32 v67, v79, v129
	global_store_dwordx4 v[148:149], v[64:67], off offset:3072
	v_mul_f32_e32 v18, v18, v144
	v_mul_f32_e32 v19, v19, v145
	s_nop 0
	v_add_co_u32_e32 v64, vcc, s10, v148
	s_movk_i32 s10, 0x2000
	s_nop 0
	v_addc_co_u32_e32 v65, vcc, 0, v149, vcc
	v_add_co_u32_e32 v66, vcc, s10, v148
	s_movk_i32 s10, 0x3000
	s_nop 0
	v_addc_co_u32_e32 v67, vcc, 0, v149, vcc
	global_store_dwordx4 v[66:67], v[32:35], off
	global_store_dwordx4 v[66:67], v[48:51], off offset:-4096
	s_nop 0
	v_mul_f32_e32 v32, v36, v132
	v_mul_f32_e32 v33, v37, v133
	v_mul_f32_e32 v34, v38, v142
	v_mul_f32_e32 v35, v39, v143
	global_store_dwordx4 v[66:67], v[32:35], off offset:1024
	v_mul_f32_e32 v48, v52, v132
	v_mul_f32_e32 v49, v53, v133
	v_mul_f32_e32 v50, v54, v142
	v_mul_f32_e32 v51, v55, v143
	v_mul_f32_e32 v32, v40, v140
	v_mul_f32_e32 v33, v41, v141
	v_mul_f32_e32 v34, v42, v134
	v_mul_f32_e32 v35, v43, v135
	global_store_dwordx4 v[66:67], v[32:35], off offset:2048
	global_store_dwordx4 v[64:65], v[48:51], off offset:1024
	s_nop 0
	v_mul_f32_e32 v32, v44, v130
	v_mul_f32_e32 v33, v45, v131
	v_mul_f32_e32 v34, v46, v128
	v_mul_f32_e32 v35, v47, v129
	global_store_dwordx4 v[66:67], v[32:35], off offset:3072
	v_mul_f32_e32 v48, v56, v140
	v_mul_f32_e32 v49, v57, v141
	v_mul_f32_e32 v50, v58, v134
	v_mul_f32_e32 v51, v59, v135
	v_add_co_u32_e32 v32, vcc, s10, v148
	global_store_dwordx4 v[64:65], v[48:51], off offset:2048
	s_nop 0
	v_addc_co_u32_e32 v33, vcc, 0, v149, vcc
	global_store_dwordx4 v[32:33], v[16:19], off
	v_mul_f32_e32 v48, v60, v130
	v_mul_f32_e32 v49, v61, v131
	v_mul_f32_e32 v50, v62, v128
	v_mul_f32_e32 v51, v63, v129
	v_mul_f32_e32 v16, v20, v132
	v_mul_f32_e32 v17, v21, v133
	v_mul_f32_e32 v18, v22, v142
	v_mul_f32_e32 v19, v23, v143
	global_store_dwordx4 v[32:33], v[16:19], off offset:1024
	global_store_dwordx4 v[64:65], v[48:51], off offset:3072
	s_nop 0
	v_mul_f32_e32 v16, v24, v140
	v_mul_f32_e32 v17, v25, v141
	v_mul_f32_e32 v18, v26, v134
	v_mul_f32_e32 v19, v27, v135
	global_store_dwordx4 v[32:33], v[16:19], off offset:2048
	s_nop 1
	v_mul_f32_e32 v16, v28, v130
	v_mul_f32_e32 v17, v29, v131
	v_mul_f32_e32 v18, v30, v128
	v_mul_f32_e32 v19, v31, v129
	global_store_dwordx4 v[32:33], v[16:19], off offset:3072

; __device__ __forceinline__ int crow(int r, int hi) { return (r & 3) + 8 * (r >> 2) + 4 * hi; }
; __device__ __forceinline__ void smax_tile(f32x16& p0, f32x16& p1, float& mhat, float& l_reg, f32x16 (&o)[4], float* al_l, const bool first, int r32, int hi,
;                                           bf16x8& pa0, bf16x8& pa1, bf16x8& pa2, bf16x8& pa3) {
;     ...
;         if (!first) { const float f = __builtin_amdgcn_exp2f(-dl); l_reg *= f;
;             if (hi == 0) al_l[r32] = f; asm volatile("s_waitcnt lgkmcnt(0)" ::: "memory");
; #pragma unroll
;             for (int d = 0; d < 4; ++d)
; #pragma unroll
;                 for (int r = 0; r < 16; ++r) o[d][r] *= al_l[crow(r, hi)]; }
.LBB0_649:
	s_or_b64 exec, exec, s[46:47]
	v_mul_f32_e32 v159, v159, v129
	s_waitcnt lgkmcnt(0)
	v_add_u32_e32 v129, s67, v154
	ds_read_b128 v[130:133], v129 offset:128
	ds_read_b128 v[162:165], v129 offset:160
	ds_read_b128 v[166:169], v129 offset:192
	ds_read_b128 v[170:173], v129 offset:224
	s_waitcnt lgkmcnt(0)
	v_mul_f32_e32 v66, v66, v132
	v_mul_f32_e32 v67, v67, v133
	v_mul_f32_e32 v68, v68, v162
	v_mul_f32_e32 v69, v69, v163
	v_mul_f32_e32 v72, v72, v166
	v_mul_f32_e32 v73, v73, v167
	v_mul_f32_e32 v76, v76, v170
	v_mul_f32_e32 v77, v77, v171
	v_mul_f32_e32 v78, v78, v172
	v_mul_f32_e32 v79, v79, v173
	v_mul_f32_e32 v74, v74, v168
	v_mul_f32_e32 v75, v75, v169
	v_mul_f32_e32 v70, v70, v164
	v_mul_f32_e32 v71, v71, v165
	v_mul_f32_e32 v64, v64, v130
	v_mul_f32_e32 v65, v65, v131
	v_mul_f32_e32 v60, v170, v60
	v_mul_f32_e32 v61, v171, v61
	v_mul_f32_e32 v56, v166, v56
	v_mul_f32_e32 v57, v167, v57
	v_mul_f32_e32 v52, v162, v52
	v_mul_f32_e32 v53, v163, v53
	v_mul_f32_e32 v62, v172, v62
	v_mul_f32_e32 v63, v173, v63
	v_mul_f32_e32 v58, v168, v58
	v_mul_f32_e32 v59, v169, v59
	v_mul_f32_e32 v54, v164, v54
	v_mul_f32_e32 v55, v165, v55
	v_mul_f32_e32 v50, v132, v50
	v_mul_f32_e32 v51, v133, v51
	v_mul_f32_e32 v48, v130, v48
	v_mul_f32_e32 v49, v131, v49
	v_mul_f32_e32 v44, v170, v44
	v_mul_f32_e32 v45, v171, v45
	v_mul_f32_e32 v40, v166, v40
	v_mul_f32_e32 v41, v167, v41
	v_mul_f32_e32 v36, v162, v36
	v_mul_f32_e32 v37, v163, v37
	v_mul_f32_e32 v46, v172, v46
	v_mul_f32_e32 v47, v173, v47
	v_mul_f32_e32 v42, v168, v42
	v_mul_f32_e32 v43, v169, v43
	v_mul_f32_e32 v38, v164, v38
	v_mul_f32_e32 v39, v165, v39
	v_mul_f32_e32 v34, v132, v34
	v_mul_f32_e32 v35, v133, v35
	v_mul_f32_e32 v32, v130, v32
	v_mul_f32_e32 v33, v131, v33
	v_mul_f32_e32 v28, v170, v28
	v_mul_f32_e32 v29, v171, v29
	v_mul_f32_e32 v24, v166, v24
	v_mul_f32_e32 v25, v167, v25
	v_mul_f32_e32 v20, v162, v20
	v_mul_f32_e32 v21, v163, v21
	v_mul_f32_e32 v30, v172, v30
	v_mul_f32_e32 v31, v173, v31
	v_mul_f32_e32 v26, v168, v26
	v_mul_f32_e32 v27, v169, v27
	v_mul_f32_e32 v22, v164, v22
	v_mul_f32_e32 v23, v165, v23
	v_mul_f32_e32 v18, v132, v18
	v_mul_f32_e32 v19, v133, v19
	v_mul_f32_e32 v16, v130, v16
	v_mul_f32_e32 v17, v131, v17

; __device__ __forceinline__ int crow(int r, int hi) { return (r & 3) + 8 * (r >> 2) + 4 * hi; }
; __device__ __forceinline__ void smax_tile(f32x16& p0, f32x16& p1, float& mhat, float& l_reg, f32x16 (&o)[4], float* al_l, const bool first, int r32, int hi,
;                                           bf16x8& pa0, bf16x8& pa1, bf16x8& pa2, bf16x8& pa3) {
;     ...
;     if (__builtin_expect(first || __any(rm > THRL), 0)) {
;         const float dl = first ? rm : fmaxf(rm, 0.f);
;         mhat += dl;
; #pragma unroll
;         for (int r = 0; r < 16; ++r) { p0[r] -= dl; p1[r] -= dl; }
;         if (!first) { const float f = __builtin_amdgcn_exp2f(-dl); l_reg *= f;
;             if (hi == 0) al_l[r32] = f; asm volatile("s_waitcnt lgkmcnt(0)" ::: "memory");
; #pragma unroll
;             for (int d = 0; d < 4; ++d)
; #pragma unroll
;                 for (int r = 0; r < 16; ++r) o[d][r] *= al_l[crow(r, hi)]; }
.LBB0_678:
	v_max_f32_e32 v120, v120, v120
	v_max_f32_e32 v120, 0, v120
	v_exp_f32_e64 v121, -v120
	s_and_saveexec_b64 s[12:13], s[10:11]
	ds_write_b32 v155, v121 offset:128
	s_or_b64 exec, exec, s[12:13]
	s_waitcnt lgkmcnt(0)
	v_add_u32_e32 v134, s67, v154
	ds_read_b128 v[122:125], v134 offset:192
	ds_read_b128 v[126:129], v134 offset:224
	ds_read_b128 v[130:133], v134 offset:128
	ds_read_b128 v[140:143], v134 offset:160
	v_add_f32_e32 v158, v158, v120
	v_add_f32_e64 v96, v96, -v120
	v_add_f32_e64 v97, v97, -v120
	v_add_f32_e64 v80, v80, -v120
	v_add_f32_e64 v81, v81, -v120
	v_add_f32_e64 v98, v98, -v120
	v_add_f32_e64 v99, v99, -v120
	v_add_f32_e64 v82, v82, -v120
	v_add_f32_e64 v83, v83, -v120
	v_add_f32_e64 v100, v100, -v120
	v_add_f32_e64 v101, v101, -v120
	v_add_f32_e64 v84, v84, -v120
	v_add_f32_e64 v85, v85, -v120
	v_add_f32_e64 v102, v102, -v120
	v_add_f32_e64 v103, v103, -v120
	v_add_f32_e64 v86, v86, -v120
	v_add_f32_e64 v87, v87, -v120
	v_add_f32_e64 v104, v104, -v120
	v_add_f32_e64 v105, v105, -v120
	v_add_f32_e64 v88, v88, -v120
	v_add_f32_e64 v89, v89, -v120
	v_add_f32_e64 v106, v106, -v120
	v_add_f32_e64 v107, v107, -v120
	v_add_f32_e64 v90, v90, -v120
	v_add_f32_e64 v91, v91, -v120
	v_add_f32_e64 v108, v108, -v120
	v_add_f32_e64 v109, v109, -v120
	v_add_f32_e64 v92, v92, -v120
	v_add_f32_e64 v93, v93, -v120
	v_add_f32_e64 v110, v110, -v120
	v_add_f32_e64 v111, v111, -v120
	v_add_f32_e64 v94, v94, -v120
	v_add_f32_e64 v95, v95, -v120
	v_mul_f32_e32 v159, v159, v121
	s_waitcnt lgkmcnt(0)
	v_mul_f32_e32 v76, v76, v126
	v_mul_f32_e32 v77, v77, v127
	v_mul_f32_e32 v72, v72, v122
	v_mul_f32_e32 v73, v73, v123
	v_mul_f32_e32 v68, v68, v140
	v_mul_f32_e32 v69, v69, v141
	v_mul_f32_e32 v78, v78, v128
	v_mul_f32_e32 v79, v79, v129
	v_mul_f32_e32 v74, v74, v124
	v_mul_f32_e32 v75, v75, v125
	v_mul_f32_e32 v70, v70, v142
	v_mul_f32_e32 v71, v71, v143
	v_mul_f32_e32 v66, v66, v132
	v_mul_f32_e32 v67, v67, v133
	v_mul_f32_e32 v64, v64, v130
	v_mul_f32_e32 v65, v65, v131
	v_mul_f32_e32 v60, v126, v60
	v_mul_f32_e32 v61, v127, v61
	v_mul_f32_e32 v56, v122, v56
	v_mul_f32_e32 v57, v123, v57
	v_mul_f32_e32 v52, v140, v52
	v_mul_f32_e32 v53, v141, v53
	v_mul_f32_e32 v62, v128, v62
	v_mul_f32_e32 v63, v129, v63
	v_mul_f32_e32 v58, v124, v58
	v_mul_f32_e32 v59, v125, v59
	v_mul_f32_e32 v54, v142, v54
	v_mul_f32_e32 v55, v143, v55
	v_mul_f32_e32 v50, v132, v50
	v_mul_f32_e32 v51, v133, v51
	v_mul_f32_e32 v48, v130, v48
	v_mul_f32_e32 v49, v131, v49
	v_mul_f32_e32 v44, v126, v44
	v_mul_f32_e32 v45, v127, v45
	v_mul_f32_e32 v40, v122, v40
	v_mul_f32_e32 v41, v123, v41
	v_mul_f32_e32 v36, v140, v36
	v_mul_f32_e32 v37, v141, v37
	v_mul_f32_e32 v46, v128, v46
	v_mul_f32_e32 v47, v129, v47
	v_mul_f32_e32 v42, v124, v42
	v_mul_f32_e32 v43, v125, v43
	v_mul_f32_e32 v38, v142, v38
	v_mul_f32_e32 v39, v143, v39
	v_mul_f32_e32 v34, v132, v34
	v_mul_f32_e32 v35, v133, v35
	v_mul_f32_e32 v32, v130, v32
	v_mul_f32_e32 v33, v131, v33
	v_mul_f32_e32 v28, v126, v28
	v_mul_f32_e32 v29, v127, v29
	v_mul_f32_e32 v24, v122, v24
	v_mul_f32_e32 v25, v123, v25
	v_mul_f32_e32 v20, v140, v20
	v_mul_f32_e32 v21, v141, v21
	v_mul_f32_e32 v30, v128, v30
	v_mul_f32_e32 v31, v129, v31
	v_mul_f32_e32 v26, v124, v26
	v_mul_f32_e32 v27, v125, v27
	v_mul_f32_e32 v22, v142, v22
	v_mul_f32_e32 v23, v143, v23
	v_mul_f32_e32 v18, v132, v18
	v_mul_f32_e32 v19, v133, v19
	v_mul_f32_e32 v16, v130, v16
	v_mul_f32_e32 v17, v131, v17
	s_branch .LBB0_667
